# attention: waves 4-7 run a rotated loop body (PV of tile t-1 first, then QK/softmax of tile t), 3 V buffers, one barrier per step; rest as v36
# speedup vs baseline: 1.0013x; 1.0013x over previous
; __device__ __forceinline__ int v_rd_base(int lane) { return ((lane & 3) << 3) | (((lane >> 2) & 3) << 6) | (((lane >> 4) & 1) << 5) | (((lane >> 5) & 1) << 8); }
; #define A3_LAS __attribute__((address_space(3)))
; __device__ __forceinline__ void block(const Blk& B, char* lds, A3_LAS unsigned char* ldsl, const int tid) {
;     const int wid = __builtin_amdgcn_readfirstlane(tid >> 6), lane = tid & 63, r32 = lane & 31, hi = lane >> 5;
;     const int NT = (B.P0 + QB3) / 64;
;     char* K_lds = lds + KOFF; char* V_lds = lds + VOFF;
;     float* sc_l = (float*)(lds + SCOFF) + wid * 64;
;     const int vb0 = (int)(uintptr_t)V_lds + attn::v_rd_base(lane);
;     const int qlo = B.P0 + wid * 32, qm = qlo + r32 - 4 * hi;
;     constexpr float C2 = 1.4426950408889634f * attn::SCALE;
;     unsigned kso[2], vso[2];
; #pragma unroll
;     for (int i = 0; i < 2; ++i) { const int row = (2 * wid + i) * 4 + (lane >> 4); const int c = (lane & 15) ^ (row & 7); kso[i] = (unsigned)(row * 128 + c * 8) * 2u; }
; #pragma unroll
;     for (int q = 0; q < 2; ++q) { const int st = 2 * (2 * wid + q) + (lane >> 5), w16 = lane & 31; const int k = (st >> 2) * 8 + (w16 >> 2);
;         const int c = (st & 3) * 32 + (w16 & 3) * 8; vso[q] = (unsigned)(k * 128 + c) * 2u; }
;     ...
;     float m_reg = -1e30f, l_reg = 0.f; bf16x8 qr[8]; f32x16 o[8] = {};
; #pragma unroll
;     for (int d0 = 0; d0 < 8; ++d0) qr[d0] = attn::load8<abf>(B.Q + (size_t)(wid * 32 + r32) * 128 + d0 * 16 + hi * 8);
;     A3_STAGE(0, 0);
;     asm volatile("s_waitcnt vmcnt(0)" ::: "memory");
;     __syncthreads();
.LBB0_323:
	s_cmp_eq_u32 s4, s94
	s_cselect_b32 s6, s95, s93
	s_lshl_b32 s17, s6, 8
	s_lshl_b32 s2, s6, 16
	v_mbcnt_lo_u32_b32 v197, -1, 0
	v_mbcnt_hi_u32_b32 v197, -1, v197
	s_add_u32 s2, s96, s2
	v_add_u32_e32 v0, s33, v197
	s_addc_u32 s3, s97, 0
	v_readfirstlane_b32 s4, v0
	s_ashr_i32 s5, s4, 6
	v_bfe_u32 v0, v197, 4, 2
	s_waitcnt vmcnt(23)
	v_lshl_or_b32 v2, s5, 3, v0
	v_bitop3_b32 v0, v0, v197, 15 bitop3:0x78
	v_lshlrev_b32_e32 v0, 4, v0
	v_and_b32_e32 v3, 15, v197
	v_lshl_or_b32 v199, v2, 8, v0
	v_or_b32_e32 v0, 4, v2
	v_bitop3_b32 v2, v0, v3, 7 bitop3:0x6c
	v_lshlrev_b32_e32 v0, 8, v0
	s_waitcnt vmcnt(21)
	v_lshlrev_b32_e32 v6, 3, v197
	v_lshl_or_b32 v200, v2, 4, v0
	v_and_b32_e32 v0, 24, v6
	v_lshlrev_b32_e32 v2, 5, v197
	v_and_b32_e32 v196, 31, v197
	s_lshl_b32 s56, s5, 5
	v_and_or_b32 v0, v197, 32, v0
	s_lshl_b32 s19, s5, 10
	v_and_b32_e32 v2, 0x380, v2
	v_or3_b32 v0, s19, v2, v0
	v_or_b32_e32 v2, s56, v196
	v_ashrrev_i32_e32 v3, 31, v2
	v_bfe_u32 v198, v197, 5, 1
	v_lshlrev_b64 v[4:5], 8, v[2:3]
	v_lshlrev_b32_e32 v201, 1, v0
	v_lshl_add_u64 v[4:5], s[2:3], 0, v[4:5]
	v_lshlrev_b32_e32 v0, 4, v198
	v_lshl_add_u64 v[4:5], v[4:5], 0, v[0:1]
	s_lshl_b32 s2, s5, 11
	v_or_b32_e32 v202, 0x80, v201
	global_load_dwordx4 v[162:165], v[4:5], off
	global_load_dwordx4 v[166:169], v[4:5], off offset:32
	global_load_dwordx4 v[170:173], v[4:5], off offset:64
	global_load_dwordx4 v[174:177], v[4:5], off offset:96
	global_load_dwordx4 v[178:181], v[4:5], off offset:128
	global_load_dwordx4 v[182:185], v[4:5], off offset:160
	global_load_dwordx4 v[186:189], v[4:5], off offset:192
	global_load_dwordx4 v[190:193], v[4:5], off offset:224
	s_add_i32 s19, s2, 0
	v_mov_b32_e32 v3, v201
	v_mov_b32_e32 v4, v200
	v_mov_b32_e32 v5, v202
	v_mov_b32_e32 v7, v199
	s_mov_b32 m0, s19
	s_and_b32 s3, s4, 0x3fffffc0
	global_load_lds_dwordx4 v7, s[46:47]
	s_add_i32 m0, s19, 0x400
	s_lshl_b32 s3, s3, 2
	global_load_lds_dwordx4 v4, s[46:47]
	s_add_i32 m0, s19, 0x8000
	s_add_i32 s2, s17, 0x100
	global_load_lds_dwordx4 v3, s[48:49]
	s_add_i32 m0, s19, 0xc000
	s_add_i32 s3, s3, 0
	global_load_lds_dwordx4 v3, s[50:51]
	s_add_i32 m0, s19, 0x8400
	s_add_i32 s4, s3, 0x20000
	global_load_lds_dwordx4 v5, s[48:49]
	s_add_i32 m0, s19, 0xc400
	s_add_i32 s23, s56, s17
	global_load_lds_dwordx4 v5, s[50:51]
	s_lshr_b32 s57, s2, 6
	v_lshlrev_b32_e32 v5, 4, v197
	v_lshlrev_b32_e32 v8, 1, v197
	s_movk_i32 s2, 0x70
	v_and_b32_e32 v8, 32, v8
	v_and_b32_e32 v9, 0x70, v5
	v_bitop3_b32 v206, v0, v5, s2 bitop3:0x78
	s_movk_i32 s2, 0x60
	v_lshl_add_u32 v204, v196, 2, s4
	v_add_u32_e32 v203, s4, v0
	s_movk_i32 s4, 0x118
	s_cmp_lg_u32 0, -1
	v_bitop3_b32 v207, v0, v9, 32 bitop3:0x36
	v_bitop3_b32 v208, v0, v9, 64 bitop3:0x36
	v_bitop3_b32 v209, v0, v9, s2 bitop3:0x36
	v_and_or_b32 v0, v6, s4, v8
	s_cselect_b32 s4, 0, 0
	v_and_b32_e32 v3, 63, v197
	v_lshlrev_b32_e32 v4, 2, v198
	v_and_b32_e32 v7, 0xc0, v5
	s_add_i32 s4, s4, 0x8000
	s_waitcnt vmcnt(0)
	v_mov_b32_e32 v14, v1
	v_mov_b32_e32 v15, v1
	s_waitcnt vmcnt(0)
	v_cmp_gt_u32_e64 s[2:3], 32, v3
	v_add3_u32 v210, v7, s4, v0
	v_sub_u32_e32 v211, v2, v4
	v_mov_b32_e32 v0, v1
	v_mov_b32_e32 v2, v1
	v_mov_b32_e32 v3, v1
	v_mov_b32_e32 v4, v1
	v_mov_b32_e32 v5, v1
	v_mov_b32_e32 v6, v1
	v_mov_b32_e32 v7, v1
	v_mov_b32_e32 v8, v1
	v_mov_b32_e32 v9, v1
	v_mov_b32_e32 v10, v1
	v_mov_b32_e32 v11, v1
	v_mov_b32_e32 v12, v1
	v_mov_b32_e32 v13, v1
	v_mov_b64_e32 v[128:129], v[14:15]
	v_mov_b64_e32 v[112:113], v[14:15]
	v_mov_b64_e32 v[96:97], v[14:15]
	v_mov_b64_e32 v[80:81], v[14:15]
	v_mov_b64_e32 v[64:65], v[14:15]
	v_mov_b64_e32 v[48:49], v[14:15]
	v_mov_b64_e32 v[32:33], v[14:15]
	v_mov_b64_e32 v[126:127], v[12:13]
	v_mov_b64_e32 v[124:125], v[10:11]
	v_mov_b64_e32 v[122:123], v[8:9]
	v_mov_b64_e32 v[120:121], v[6:7]
	v_mov_b64_e32 v[118:119], v[4:5]
	v_mov_b64_e32 v[116:117], v[2:3]
	v_mov_b64_e32 v[114:115], v[0:1]
	v_mov_b64_e32 v[110:111], v[12:13]
	v_mov_b64_e32 v[108:109], v[10:11]
	v_mov_b64_e32 v[106:107], v[8:9]
	v_mov_b64_e32 v[104:105], v[6:7]
	v_mov_b64_e32 v[102:103], v[4:5]
	v_mov_b64_e32 v[100:101], v[2:3]
	v_mov_b64_e32 v[98:99], v[0:1]
	v_mov_b64_e32 v[94:95], v[12:13]
	v_mov_b64_e32 v[92:93], v[10:11]
	v_mov_b64_e32 v[90:91], v[8:9]
	v_mov_b64_e32 v[88:89], v[6:7]
	v_mov_b64_e32 v[86:87], v[4:5]
	v_mov_b64_e32 v[84:85], v[2:3]
	v_mov_b64_e32 v[82:83], v[0:1]
	v_mov_b64_e32 v[78:79], v[12:13]
	v_mov_b64_e32 v[76:77], v[10:11]
	v_mov_b64_e32 v[74:75], v[8:9]
	v_mov_b64_e32 v[72:73], v[6:7]
	v_mov_b64_e32 v[70:71], v[4:5]
	v_mov_b64_e32 v[68:69], v[2:3]
	v_mov_b64_e32 v[66:67], v[0:1]
	v_mov_b64_e32 v[62:63], v[12:13]
	v_mov_b64_e32 v[60:61], v[10:11]
	v_mov_b64_e32 v[58:59], v[8:9]
	v_mov_b64_e32 v[56:57], v[6:7]
	v_mov_b64_e32 v[54:55], v[4:5]
	v_mov_b64_e32 v[52:53], v[2:3]
	v_mov_b64_e32 v[50:51], v[0:1]
	v_mov_b64_e32 v[46:47], v[12:13]
	v_mov_b64_e32 v[44:45], v[10:11]
	v_mov_b64_e32 v[42:43], v[8:9]
	v_mov_b64_e32 v[40:41], v[6:7]
	v_mov_b64_e32 v[38:39], v[4:5]
	v_mov_b64_e32 v[36:37], v[2:3]
	v_mov_b64_e32 v[34:35], v[0:1]
	v_mov_b64_e32 v[30:31], v[12:13]
	v_mov_b64_e32 v[28:29], v[10:11]
	v_mov_b64_e32 v[26:27], v[8:9]
	v_mov_b64_e32 v[24:25], v[6:7]
	v_mov_b64_e32 v[22:23], v[4:5]
	v_mov_b64_e32 v[20:21], v[2:3]
	v_mov_b64_e32 v[18:19], v[0:1]
	v_mov_b64_e32 v[16:17], v[14:15]
	s_mov_b32 s5, 1
	v_lshlrev_b32_e32 v205, 8, v196
	v_mov_b32_e32 v212, 0
	v_mov_b32_e32 v213, 0xf149f2ca
	s_movk_i32 s62, 0xff00
	s_mov_b64 s[58:59], s[28:29]
	v_mov_b64_e32 v[14:15], v[12:13]
	v_mov_b64_e32 v[12:13], v[10:11]
	v_mov_b64_e32 v[10:11], v[8:9]
	v_mov_b64_e32 v[8:9], v[6:7]
	v_mov_b64_e32 v[6:7], v[4:5]
	v_mov_b64_e32 v[4:5], v[2:3]
	v_mov_b64_e32 v[2:3], v[0:1]
	s_waitcnt vmcnt(0) lgkmcnt(0)
	s_barrier
	s_mov_b32 s63, 0
	s_cmp_lt_u32 s19, 0x2000
	s_cbranch_scc0 .LattB_first

; #define A3_RDK(vb, d0, s) do { A3_TRRD(xl##s, vb, (d0) * 512 + (s) * 4096); A3_TRRD(xh##s, vb, (d0) * 512 + (s) * 4096 + 2048); A3_TRRD(yl##s, vb, ((d0) + 1) * 512 + (s) * 4096); A3_TRRD(yh##s, vb, ((d0) + 1) * 512 + (s) * 4096 + 2048); } while (0)
; #define A3_PAIR(accx, accy, NEXT0, NEXT1, NEXT2, NEXT3) do { A3_STEPK(accx, accy, pa0, 0, NEXT0); A3_STEPK(accx, accy, pa1, 1, NEXT1); A3_STEPK(accx, accy, pa2, 2, NEXT2); A3_STEPK(accx, accy, pa3, 3, NEXT3); } while (0)
; #define A3_NONE do { asm volatile("s_waitcnt lgkmcnt(0)" ::: "memory"); } while (0)
; __device__ __forceinline__ float own_sum(const f32x16& P) { return ((P[0] + P[1]) + (P[2] + P[3])) + ((P[4] + P[5]) + (P[6] + P[7])) + (((P[8] + P[9]) + (P[10] + P[11])) + ((P[12] + P[13]) + (P[14] + P[15]))); }
; __device__ __forceinline__ void pv256(f32x16* o, int vb0, bf16x8 pa0, bf16x8 pa1, bf16x8 pa2, bf16x8 pa3) {
;     s16x4 xl0, xh0, xl1, xh1, xl2, xh2, xl3, xh3, yl0, yh0, yl1, yh1, yl2, yh2, yl3, yh3;
;     const int va = vb0, vb = vb0 + 16384;
;     asm volatile("s_waitcnt lgkmcnt(0)" ::: "memory");
;     A3_RDK(va, 0, 0); A3_RDK(va, 0, 1); A3_RDK(va, 0, 2); A3_RDK(va, 0, 3);
;     A3_PAIR(o[0], o[1], A3_RDK(va, 2, 0), A3_RDK(va, 2, 1), A3_RDK(va, 2, 2), A3_RDK(va, 2, 3));
;     A3_PAIR(o[2], o[3], A3_RDK(vb, 0, 0), A3_RDK(vb, 0, 1), A3_RDK(vb, 0, 2), A3_RDK(vb, 0, 3));
;     A3_PAIR(o[4], o[5], A3_RDK(vb, 2, 0), A3_RDK(vb, 2, 1), A3_RDK(vb, 2, 2), A3_RDK(vb, 2, 3));
;     A3_PAIR(o[6], o[7], A3_NONE, A3_NONE, A3_NONE, A3_NONE);
; __device__ __forceinline__ void block(const Blk& B, char* lds, A3_LAS unsigned char* ldsl, const int tid) {
;     ...
;         l_reg = l_reg * alpha + (own_sum(p0) + own_sum(p1));
;         bf16x8 pa0, pa1, pa2, pa3; pack_own(p0, pa0, pa1); pack_own(p1, pa2, pa3);
.LattA_336:
	v_add_f32_e32 v146, v217, v219
	v_add_f32_e32 v147, v221, v223
	v_add_f32_e32 v146, v146, v147
	v_add_f32_e32 v147, v226, v228
	v_add_f32_e32 v148, v230, v232
	v_add_f32_e32 v147, v147, v148
	v_add_f32_e32 v146, v146, v147
	v_add_f32_e32 v147, v233, v235
	v_add_f32_e32 v148, v238, v240
	v_add_f32_e32 v147, v147, v148
	v_add_f32_e32 v148, v242, v243
	v_add_f32_e32 v149, v244, v245
	v_add_f32_e32 v148, v148, v149
	v_add_f32_e32 v147, v147, v148
	v_add_f32_e32 v146, v146, v147
	v_add_f32_e32 v147, v213, v214
	v_add_f32_e32 v148, v215, v216
	v_add_f32_e32 v147, v147, v148
	v_add_f32_e32 v148, v218, v220
	v_add_f32_e32 v149, v222, v224
	v_add_f32_e32 v148, v148, v149
	v_add_f32_e32 v147, v147, v148
	v_add_f32_e32 v148, v225, v227
	v_add_f32_e32 v149, v229, v231
	v_add_f32_e32 v148, v148, v149
	v_add_f32_e32 v149, v234, v236
	v_add_f32_e32 v150, v239, v241
	v_add_f32_e32 v149, v149, v150
	v_add_f32_e32 v148, v148, v149
	v_add_f32_e32 v147, v147, v148
	s_waitcnt lgkmcnt(0)
	v_add_f32_e32 v146, v147, v146
	v_fmac_f32_e32 v146, v212, v237
	v_add_u32_e32 v147, s63, v210
	ds_read_b64_tr_b16 v[148:149], v147 offset:0
	ds_read_b64_tr_b16 v[150:151], v147 offset:0x800
	ds_read_b64_tr_b16 v[152:153], v147 offset:0x200
	ds_read_b64_tr_b16 v[154:155], v147 offset:0xa00
	ds_read_b64_tr_b16 v[156:157], v147 offset:0x1000
	ds_read_b64_tr_b16 v[158:159], v147 offset:0x1800
	ds_read_b64_tr_b16 v[212:213], v147 offset:0x1200
	ds_read_b64_tr_b16 v[214:215], v147 offset:0x1a00
	ds_read_b64_tr_b16 v[216:217], v147 offset:0x2000
	ds_read_b64_tr_b16 v[218:219], v147 offset:0x2800
	ds_read_b64_tr_b16 v[220:221], v147 offset:0x2200
	ds_read_b64_tr_b16 v[222:223], v147 offset:0x2a00
	ds_read_b64_tr_b16 v[224:225], v147 offset:0x3000
	ds_read_b64_tr_b16 v[226:227], v147 offset:0x3800
	ds_read_b64_tr_b16 v[228:229], v147 offset:0x3200
	ds_read_b64_tr_b16 v[230:231], v147 offset:0x3a00
	s_waitcnt lgkmcnt(12)
	v_add_u32_e32 v160, 0x4000, v147
	v_mfma_f32_32x32x16_bf16 v[114:129], v[142:145], v[148:151], v[114:129]
	v_mfma_f32_32x32x16_bf16 v[98:113], v[142:145], v[152:155], v[98:113]
	ds_read_b64_tr_b16 v[148:149], v147 offset:0x400
	ds_read_b64_tr_b16 v[150:151], v147 offset:0xc00
	ds_read_b64_tr_b16 v[152:153], v147 offset:0x600
	ds_read_b64_tr_b16 v[154:155], v147 offset:0xe00
	s_waitcnt lgkmcnt(12)
	v_mfma_f32_32x32x16_bf16 v[114:129], v[138:141], v[156:159], v[114:129]
	v_mfma_f32_32x32x16_bf16 v[98:113], v[138:141], v[212:215], v[98:113]
	ds_read_b64_tr_b16 v[156:157], v147 offset:0x1400
	ds_read_b64_tr_b16 v[158:159], v147 offset:0x1c00
	ds_read_b64_tr_b16 v[212:213], v147 offset:0x1600
	ds_read_b64_tr_b16 v[214:215], v147 offset:0x1e00
	s_waitcnt lgkmcnt(12)
	v_mfma_f32_32x32x16_bf16 v[114:129], v[134:137], v[216:219], v[114:129]
	v_mfma_f32_32x32x16_bf16 v[98:113], v[134:137], v[220:223], v[98:113]
	ds_read_b64_tr_b16 v[216:217], v147 offset:0x2400
	ds_read_b64_tr_b16 v[218:219], v147 offset:0x2c00
	ds_read_b64_tr_b16 v[220:221], v147 offset:0x2600
	ds_read_b64_tr_b16 v[222:223], v147 offset:0x2e00
	s_waitcnt lgkmcnt(12)
	v_mfma_f32_32x32x16_bf16 v[114:129], v[130:133], v[224:227], v[114:129]
	v_mfma_f32_32x32x16_bf16 v[98:113], v[130:133], v[228:231], v[98:113]
	ds_read_b64_tr_b16 v[224:225], v147 offset:0x3400
	ds_read_b64_tr_b16 v[226:227], v147 offset:0x3c00
	ds_read_b64_tr_b16 v[228:229], v147 offset:0x3600
	ds_read_b64_tr_b16 v[230:231], v147 offset:0x3e00
	s_waitcnt lgkmcnt(12)
	v_mfma_f32_32x32x16_bf16 v[82:97], v[142:145], v[148:151], v[82:97]
	v_mfma_f32_32x32x16_bf16 v[66:81], v[142:145], v[152:155], v[66:81]
	ds_read_b64_tr_b16 v[148:149], v160 offset:0
	ds_read_b64_tr_b16 v[150:151], v160 offset:0x800
	ds_read_b64_tr_b16 v[152:153], v160 offset:0x200
	ds_read_b64_tr_b16 v[154:155], v160 offset:0xa00
	s_waitcnt lgkmcnt(12)
	v_mfma_f32_32x32x16_bf16 v[82:97], v[138:141], v[156:159], v[82:97]
	v_mfma_f32_32x32x16_bf16 v[66:81], v[138:141], v[212:215], v[66:81]
	ds_read_b64_tr_b16 v[156:157], v160 offset:0x1000
	ds_read_b64_tr_b16 v[158:159], v160 offset:0x1800
	ds_read_b64_tr_b16 v[212:213], v160 offset:0x1200
	ds_read_b64_tr_b16 v[214:215], v160 offset:0x1a00
	s_waitcnt lgkmcnt(12)
	v_mfma_f32_32x32x16_bf16 v[82:97], v[134:137], v[216:219], v[82:97]
	v_mfma_f32_32x32x16_bf16 v[66:81], v[134:137], v[220:223], v[66:81]
	ds_read_b64_tr_b16 v[216:217], v160 offset:0x2000
	ds_read_b64_tr_b16 v[218:219], v160 offset:0x2800
	ds_read_b64_tr_b16 v[220:221], v160 offset:0x2200
	ds_read_b64_tr_b16 v[222:223], v160 offset:0x2a00
	s_waitcnt lgkmcnt(12)
	v_mfma_f32_32x32x16_bf16 v[82:97], v[130:133], v[224:227], v[82:97]
	v_mfma_f32_32x32x16_bf16 v[66:81], v[130:133], v[228:231], v[66:81]
	ds_read_b64_tr_b16 v[224:225], v160 offset:0x3000
	ds_read_b64_tr_b16 v[226:227], v160 offset:0x3800
	ds_read_b64_tr_b16 v[228:229], v160 offset:0x3200
	ds_read_b64_tr_b16 v[230:231], v160 offset:0x3a00
	s_waitcnt lgkmcnt(12)
	v_mfma_f32_32x32x16_bf16 v[50:65], v[142:145], v[148:151], v[50:65]
	v_mfma_f32_32x32x16_bf16 v[34:49], v[142:145], v[152:155], v[34:49]
	ds_read_b64_tr_b16 v[148:149], v160 offset:0x400
	ds_read_b64_tr_b16 v[150:151], v160 offset:0xc00
	ds_read_b64_tr_b16 v[152:153], v160 offset:0x600
	ds_read_b64_tr_b16 v[154:155], v160 offset:0xe00
	s_waitcnt lgkmcnt(12)
	v_mfma_f32_32x32x16_bf16 v[50:65], v[138:141], v[156:159], v[50:65]
	v_mfma_f32_32x32x16_bf16 v[34:49], v[138:141], v[212:215], v[34:49]
	ds_read_b64_tr_b16 v[156:157], v160 offset:0x1400
	ds_read_b64_tr_b16 v[158:159], v160 offset:0x1c00
	ds_read_b64_tr_b16 v[212:213], v160 offset:0x1600
	ds_read_b64_tr_b16 v[214:215], v160 offset:0x1e00
	s_waitcnt lgkmcnt(12)
; #define A3_RDK(vb, d0, s) do { A3_TRRD(xl##s, vb, (d0) * 512 + (s) * 4096); A3_TRRD(xh##s, vb, (d0) * 512 + (s) * 4096 + 2048); A3_TRRD(yl##s, vb, ((d0) + 1) * 512 + (s) * 4096); A3_TRRD(yh##s, vb, ((d0) + 1) * 512 + (s) * 4096 + 2048); } while (0)
; #define A3_PAIR(accx, accy, NEXT0, NEXT1, NEXT2, NEXT3) do { A3_STEPK(accx, accy, pa0, 0, NEXT0); A3_STEPK(accx, accy, pa1, 1, NEXT1); A3_STEPK(accx, accy, pa2, 2, NEXT2); A3_STEPK(accx, accy, pa3, 3, NEXT3); } while (0)
; #define A3_NONE do { asm volatile("s_waitcnt lgkmcnt(0)" ::: "memory"); } while (0)
; __device__ __forceinline__ void pv256(f32x16* o, int vb0, bf16x8 pa0, bf16x8 pa1, bf16x8 pa2, bf16x8 pa3) {
;     ...
;     A3_PAIR(o[0], o[1], A3_RDK(va, 2, 0), A3_RDK(va, 2, 1), A3_RDK(va, 2, 2), A3_RDK(va, 2, 3));
;     A3_PAIR(o[2], o[3], A3_RDK(vb, 0, 0), A3_RDK(vb, 0, 1), A3_RDK(vb, 0, 2), A3_RDK(vb, 0, 3));
;     A3_PAIR(o[4], o[5], A3_RDK(vb, 2, 0), A3_RDK(vb, 2, 1), A3_RDK(vb, 2, 2), A3_RDK(vb, 2, 3));
;     A3_PAIR(o[6], o[7], A3_NONE, A3_NONE, A3_NONE, A3_NONE);
; __device__ __forceinline__ void block(const Blk& B, char* lds, A3_LAS unsigned char* ldsl, const int tid) {
;     ...
;         pv256(o, vb0 + buf * 32768, pa0, pa1, pa2, pa3);
;         asm volatile("s_waitcnt vmcnt(0)" ::: "memory");
;         __syncthreads();
;     }
	v_mfma_f32_32x32x16_bf16 v[50:65], v[134:137], v[216:219], v[50:65]
	v_mfma_f32_32x32x16_bf16 v[34:49], v[134:137], v[220:223], v[34:49]
	ds_read_b64_tr_b16 v[216:217], v160 offset:0x2400
	ds_read_b64_tr_b16 v[218:219], v160 offset:0x2c00
	ds_read_b64_tr_b16 v[220:221], v160 offset:0x2600
	ds_read_b64_tr_b16 v[222:223], v160 offset:0x2e00
	s_waitcnt lgkmcnt(12)
	v_mfma_f32_32x32x16_bf16 v[50:65], v[130:133], v[224:227], v[50:65]
	v_mfma_f32_32x32x16_bf16 v[34:49], v[130:133], v[228:231], v[34:49]
	ds_read_b64_tr_b16 v[224:225], v160 offset:0x3400
	ds_read_b64_tr_b16 v[226:227], v160 offset:0x3c00
	ds_read_b64_tr_b16 v[228:229], v160 offset:0x3600
	ds_read_b64_tr_b16 v[230:231], v160 offset:0x3e00
	s_waitcnt lgkmcnt(12)
	v_mfma_f32_32x32x16_bf16 v[18:33], v[142:145], v[148:151], v[18:33]
	v_mfma_f32_32x32x16_bf16 v[2:17], v[142:145], v[152:155], v[2:17]
	s_waitcnt lgkmcnt(0)
	s_waitcnt lgkmcnt(12)
	v_mfma_f32_32x32x16_bf16 v[18:33], v[138:141], v[156:159], v[18:33]
	v_mfma_f32_32x32x16_bf16 v[2:17], v[138:141], v[212:215], v[2:17]
	s_waitcnt lgkmcnt(0)
	s_waitcnt lgkmcnt(12)
	v_mfma_f32_32x32x16_bf16 v[18:33], v[134:137], v[216:219], v[18:33]
	v_mfma_f32_32x32x16_bf16 v[2:17], v[134:137], v[220:223], v[2:17]
	s_waitcnt lgkmcnt(0)
	s_waitcnt lgkmcnt(12)
	v_mfma_f32_32x32x16_bf16 v[18:33], v[130:133], v[224:227], v[18:33]
	v_mfma_f32_32x32x16_bf16 v[2:17], v[130:133], v[228:231], v[2:17]
	s_waitcnt lgkmcnt(0)
	s_waitcnt vmcnt(0)
	s_add_u32 s58, s58, 0x4000
	s_addc_u32 s59, s59, 0
	s_add_i32 s62, s62, 64
	s_add_i32 s5, s5, 1
	s_mov_b32 s65, s63
	s_add_i32 s63, s63, 0x8000
	s_cmp_eq_u32 s63, 0x18000
	s_cselect_b32 s63, 0, s63
	v_subrev_u32_e32 v211, 64, v211
	s_cmp_eq_u32 s17, s62
	s_barrier
	s_cbranch_scc1 .LBB0_338
	v_mov_b32_e32 v213, v0
	v_mov_b32_e32 v212, v146
	s_branch .LBB0_324
; #define A3_RDK(vb, d0, s) do { A3_TRRD(xl##s, vb, (d0) * 512 + (s) * 4096); A3_TRRD(xh##s, vb, (d0) * 512 + (s) * 4096 + 2048); A3_TRRD(yl##s, vb, ((d0) + 1) * 512 + (s) * 4096); A3_TRRD(yh##s, vb, ((d0) + 1) * 512 + (s) * 4096 + 2048); } while (0)
; #define A3_PAIR(accx, accy, NEXT0, NEXT1, NEXT2, NEXT3) do { A3_STEPK(accx, accy, pa0, 0, NEXT0); A3_STEPK(accx, accy, pa1, 1, NEXT1); A3_STEPK(accx, accy, pa2, 2, NEXT2); A3_STEPK(accx, accy, pa3, 3, NEXT3); } while (0)
; #define A3_NONE do { asm volatile("s_waitcnt lgkmcnt(0)" ::: "memory"); } while (0)
; __device__ __forceinline__ void pv256(f32x16* o, int vb0, bf16x8 pa0, bf16x8 pa1, bf16x8 pa2, bf16x8 pa3) {
;     s16x4 xl0, xh0, xl1, xh1, xl2, xh2, xl3, xh3, yl0, yh0, yl1, yh1, yl2, yh2, yl3, yh3;
;     const int va = vb0, vb = vb0 + 16384;
;     asm volatile("s_waitcnt lgkmcnt(0)" ::: "memory");
;     A3_RDK(va, 0, 0); A3_RDK(va, 0, 1); A3_RDK(va, 0, 2); A3_RDK(va, 0, 3);
;     A3_PAIR(o[0], o[1], A3_RDK(va, 2, 0), A3_RDK(va, 2, 1), A3_RDK(va, 2, 2), A3_RDK(va, 2, 3));
;     A3_PAIR(o[2], o[3], A3_RDK(vb, 0, 0), A3_RDK(vb, 0, 1), A3_RDK(vb, 0, 2), A3_RDK(vb, 0, 3));
;     A3_PAIR(o[4], o[5], A3_RDK(vb, 2, 0), A3_RDK(vb, 2, 1), A3_RDK(vb, 2, 2), A3_RDK(vb, 2, 3));
;     A3_PAIR(o[6], o[7], A3_NONE, A3_NONE, A3_NONE, A3_NONE);
; }
; __device__ __forceinline__ void block(const Blk& B, char* lds, A3_LAS unsigned char* ldsl, const int tid) {
;     ...
;         pv256(o, vb0 + buf * 32768, pa0, pa1, pa2, pa3);
.LattB_head:
	v_add_u32_e32 v147, s65, v210
	ds_read_b64_tr_b16 v[148:149], v147 offset:0
	ds_read_b64_tr_b16 v[150:151], v147 offset:0x800
	ds_read_b64_tr_b16 v[152:153], v147 offset:0x200
	ds_read_b64_tr_b16 v[154:155], v147 offset:0xa00
	ds_read_b64_tr_b16 v[156:157], v147 offset:0x1000
	ds_read_b64_tr_b16 v[158:159], v147 offset:0x1800
	ds_read_b64_tr_b16 v[212:213], v147 offset:0x1200
	ds_read_b64_tr_b16 v[214:215], v147 offset:0x1a00
	ds_read_b64_tr_b16 v[216:217], v147 offset:0x2000
	ds_read_b64_tr_b16 v[218:219], v147 offset:0x2800
	ds_read_b64_tr_b16 v[220:221], v147 offset:0x2200
	ds_read_b64_tr_b16 v[222:223], v147 offset:0x2a00
	ds_read_b64_tr_b16 v[224:225], v147 offset:0x3000
	ds_read_b64_tr_b16 v[226:227], v147 offset:0x3800
	ds_read_b64_tr_b16 v[228:229], v147 offset:0x3200
	ds_read_b64_tr_b16 v[230:231], v147 offset:0x3a00
	s_waitcnt lgkmcnt(12)
	v_add_u32_e32 v160, 0x4000, v147
	v_mfma_f32_32x32x16_bf16 v[114:129], v[142:145], v[148:151], v[114:129]
	v_mfma_f32_32x32x16_bf16 v[98:113], v[142:145], v[152:155], v[98:113]
	ds_read_b64_tr_b16 v[148:149], v147 offset:0x400
	ds_read_b64_tr_b16 v[150:151], v147 offset:0xc00
	ds_read_b64_tr_b16 v[152:153], v147 offset:0x600
	ds_read_b64_tr_b16 v[154:155], v147 offset:0xe00
	s_waitcnt lgkmcnt(12)
	v_mfma_f32_32x32x16_bf16 v[114:129], v[138:141], v[156:159], v[114:129]
	v_mfma_f32_32x32x16_bf16 v[98:113], v[138:141], v[212:215], v[98:113]
	ds_read_b64_tr_b16 v[156:157], v147 offset:0x1400
	ds_read_b64_tr_b16 v[158:159], v147 offset:0x1c00
	ds_read_b64_tr_b16 v[212:213], v147 offset:0x1600
	ds_read_b64_tr_b16 v[214:215], v147 offset:0x1e00
	s_waitcnt lgkmcnt(12)
	v_mfma_f32_32x32x16_bf16 v[114:129], v[134:137], v[216:219], v[114:129]
	v_mfma_f32_32x32x16_bf16 v[98:113], v[134:137], v[220:223], v[98:113]
	ds_read_b64_tr_b16 v[216:217], v147 offset:0x2400
	ds_read_b64_tr_b16 v[218:219], v147 offset:0x2c00
	ds_read_b64_tr_b16 v[220:221], v147 offset:0x2600
	ds_read_b64_tr_b16 v[222:223], v147 offset:0x2e00
	s_waitcnt lgkmcnt(12)
	v_mfma_f32_32x32x16_bf16 v[114:129], v[130:133], v[224:227], v[114:129]
	v_mfma_f32_32x32x16_bf16 v[98:113], v[130:133], v[228:231], v[98:113]
	ds_read_b64_tr_b16 v[224:225], v147 offset:0x3400
	ds_read_b64_tr_b16 v[226:227], v147 offset:0x3c00
	ds_read_b64_tr_b16 v[228:229], v147 offset:0x3600
	ds_read_b64_tr_b16 v[230:231], v147 offset:0x3e00
	s_waitcnt lgkmcnt(12)
	v_mfma_f32_32x32x16_bf16 v[82:97], v[142:145], v[148:151], v[82:97]
	v_mfma_f32_32x32x16_bf16 v[66:81], v[142:145], v[152:155], v[66:81]
	ds_read_b64_tr_b16 v[148:149], v160 offset:0
	ds_read_b64_tr_b16 v[150:151], v160 offset:0x800
	ds_read_b64_tr_b16 v[152:153], v160 offset:0x200
	ds_read_b64_tr_b16 v[154:155], v160 offset:0xa00
	s_waitcnt lgkmcnt(12)
	v_mfma_f32_32x32x16_bf16 v[82:97], v[138:141], v[156:159], v[82:97]
	v_mfma_f32_32x32x16_bf16 v[66:81], v[138:141], v[212:215], v[66:81]
	ds_read_b64_tr_b16 v[156:157], v160 offset:0x1000
	ds_read_b64_tr_b16 v[158:159], v160 offset:0x1800
	ds_read_b64_tr_b16 v[212:213], v160 offset:0x1200
	ds_read_b64_tr_b16 v[214:215], v160 offset:0x1a00
	s_waitcnt lgkmcnt(12)
	v_mfma_f32_32x32x16_bf16 v[82:97], v[134:137], v[216:219], v[82:97]
	v_mfma_f32_32x32x16_bf16 v[66:81], v[134:137], v[220:223], v[66:81]
	ds_read_b64_tr_b16 v[216:217], v160 offset:0x2000
	ds_read_b64_tr_b16 v[218:219], v160 offset:0x2800
	ds_read_b64_tr_b16 v[220:221], v160 offset:0x2200
	ds_read_b64_tr_b16 v[222:223], v160 offset:0x2a00
	s_waitcnt lgkmcnt(12)
	v_mfma_f32_32x32x16_bf16 v[82:97], v[130:133], v[224:227], v[82:97]
	v_mfma_f32_32x32x16_bf16 v[66:81], v[130:133], v[228:231], v[66:81]
	ds_read_b64_tr_b16 v[224:225], v160 offset:0x3000
	ds_read_b64_tr_b16 v[226:227], v160 offset:0x3800
	ds_read_b64_tr_b16 v[228:229], v160 offset:0x3200
	ds_read_b64_tr_b16 v[230:231], v160 offset:0x3a00
	s_waitcnt lgkmcnt(12)
	v_mfma_f32_32x32x16_bf16 v[50:65], v[142:145], v[148:151], v[50:65]
	v_mfma_f32_32x32x16_bf16 v[34:49], v[142:145], v[152:155], v[34:49]
	ds_read_b64_tr_b16 v[148:149], v160 offset:0x400
	ds_read_b64_tr_b16 v[150:151], v160 offset:0xc00
	ds_read_b64_tr_b16 v[152:153], v160 offset:0x600
	ds_read_b64_tr_b16 v[154:155], v160 offset:0xe00
	s_waitcnt lgkmcnt(12)
	v_mfma_f32_32x32x16_bf16 v[50:65], v[138:141], v[156:159], v[50:65]
	v_mfma_f32_32x32x16_bf16 v[34:49], v[138:141], v[212:215], v[34:49]
	ds_read_b64_tr_b16 v[156:157], v160 offset:0x1400
	ds_read_b64_tr_b16 v[158:159], v160 offset:0x1c00
	ds_read_b64_tr_b16 v[212:213], v160 offset:0x1600
	ds_read_b64_tr_b16 v[214:215], v160 offset:0x1e00
	s_waitcnt lgkmcnt(12)
	v_mfma_f32_32x32x16_bf16 v[50:65], v[134:137], v[216:219], v[50:65]
	v_mfma_f32_32x32x16_bf16 v[34:49], v[134:137], v[220:223], v[34:49]
	ds_read_b64_tr_b16 v[216:217], v160 offset:0x2400
	ds_read_b64_tr_b16 v[218:219], v160 offset:0x2c00
	ds_read_b64_tr_b16 v[220:221], v160 offset:0x2600
	ds_read_b64_tr_b16 v[222:223], v160 offset:0x2e00
	s_waitcnt lgkmcnt(12)
	v_mfma_f32_32x32x16_bf16 v[50:65], v[130:133], v[224:227], v[50:65]
	v_mfma_f32_32x32x16_bf16 v[34:49], v[130:133], v[228:231], v[34:49]
	ds_read_b64_tr_b16 v[224:225], v160 offset:0x3400
	ds_read_b64_tr_b16 v[226:227], v160 offset:0x3c00
	ds_read_b64_tr_b16 v[228:229], v160 offset:0x3600
	ds_read_b64_tr_b16 v[230:231], v160 offset:0x3e00
	s_waitcnt lgkmcnt(12)
	v_mfma_f32_32x32x16_bf16 v[18:33], v[142:145], v[148:151], v[18:33]
	v_mfma_f32_32x32x16_bf16 v[2:17], v[142:145], v[152:155], v[2:17]
	s_waitcnt lgkmcnt(0)
	s_waitcnt lgkmcnt(12)
	v_mfma_f32_32x32x16_bf16 v[18:33], v[138:141], v[156:159], v[18:33]
	v_mfma_f32_32x32x16_bf16 v[2:17], v[138:141], v[212:215], v[2:17]
	s_waitcnt lgkmcnt(0)
	s_waitcnt lgkmcnt(12)
	v_mfma_f32_32x32x16_bf16 v[18:33], v[134:137], v[216:219], v[18:33]
	v_mfma_f32_32x32x16_bf16 v[2:17], v[134:137], v[220:223], v[2:17]
	s_waitcnt lgkmcnt(0)
	s_waitcnt lgkmcnt(12)
	v_mfma_f32_32x32x16_bf16 v[18:33], v[130:133], v[224:227], v[18:33]
	v_mfma_f32_32x32x16_bf16 v[2:17], v[130:133], v[228:231], v[2:17]
	s_waitcnt lgkmcnt(0)
	v_mov_b32_e32 v213, v0
	v_mov_b32_e32 v212, v146

; __device__ __forceinline__ float own_sum(const f32x16& P) { return ((P[0] + P[1]) + (P[2] + P[3])) + ((P[4] + P[5]) + (P[6] + P[7])) + (((P[8] + P[9]) + (P[10] + P[11])) + ((P[12] + P[13]) + (P[14] + P[15]))); }
; __device__ __forceinline__ void block(const Blk& B, char* lds, A3_LAS unsigned char* ldsl, const int tid) {
;     ...
;         l_reg = l_reg * alpha + (own_sum(p0) + own_sum(p1));
;         bf16x8 pa0, pa1, pa2, pa3; pack_own(p0, pa0, pa1); pack_own(p1, pa2, pa3);
;     ...
;         asm volatile("s_waitcnt vmcnt(0)" ::: "memory");
;         __syncthreads();
;     }
.LattB_336:
	v_add_f32_e32 v146, v217, v219
	v_add_f32_e32 v147, v221, v223
	v_add_f32_e32 v146, v146, v147
	v_add_f32_e32 v147, v226, v228
	v_add_f32_e32 v148, v230, v232
	v_add_f32_e32 v147, v147, v148
	v_add_f32_e32 v146, v146, v147
	v_add_f32_e32 v147, v233, v235
	v_add_f32_e32 v148, v238, v240
	v_add_f32_e32 v147, v147, v148
	v_add_f32_e32 v148, v242, v243
	v_add_f32_e32 v149, v244, v245
	v_add_f32_e32 v148, v148, v149
	v_add_f32_e32 v147, v147, v148
	v_add_f32_e32 v146, v146, v147
	v_add_f32_e32 v147, v213, v214
	v_add_f32_e32 v148, v215, v216
	v_add_f32_e32 v147, v147, v148
	v_add_f32_e32 v148, v218, v220
	v_add_f32_e32 v149, v222, v224
	v_add_f32_e32 v148, v148, v149
	v_add_f32_e32 v147, v147, v148
	v_add_f32_e32 v148, v225, v227
	v_add_f32_e32 v149, v229, v231
	v_add_f32_e32 v148, v148, v149
	v_add_f32_e32 v149, v234, v236
	v_add_f32_e32 v150, v239, v241
	v_add_f32_e32 v149, v149, v150
	v_add_f32_e32 v148, v148, v149
	v_add_f32_e32 v147, v147, v148
	s_waitcnt lgkmcnt(0)
	v_add_f32_e32 v146, v147, v146
	v_fmac_f32_e32 v146, v212, v237
	s_waitcnt vmcnt(0)
	s_add_u32 s58, s58, 0x4000
	s_addc_u32 s59, s59, 0
	s_add_i32 s62, s62, 64
	s_add_i32 s5, s5, 1
	s_mov_b32 s65, s63
	s_add_i32 s63, s63, 0x8000
	s_cmp_eq_u32 s63, 0x18000
	s_cselect_b32 s63, 0, s63
	v_subrev_u32_e32 v211, 64, v211
	s_cmp_eq_u32 s17, s62
	s_barrier
	s_cbranch_scc1 .LattB_exit
	s_branch .LattB_head
; #define A3_RDK(vb, d0, s) do { A3_TRRD(xl##s, vb, (d0) * 512 + (s) * 4096); A3_TRRD(xh##s, vb, (d0) * 512 + (s) * 4096 + 2048); A3_TRRD(yl##s, vb, ((d0) + 1) * 512 + (s) * 4096); A3_TRRD(yh##s, vb, ((d0) + 1) * 512 + (s) * 4096 + 2048); } while (0)
; #define A3_PAIR(accx, accy, NEXT0, NEXT1, NEXT2, NEXT3) do { A3_STEPK(accx, accy, pa0, 0, NEXT0); A3_STEPK(accx, accy, pa1, 1, NEXT1); A3_STEPK(accx, accy, pa2, 2, NEXT2); A3_STEPK(accx, accy, pa3, 3, NEXT3); } while (0)
; #define A3_NONE do { asm volatile("s_waitcnt lgkmcnt(0)" ::: "memory"); } while (0)
; __device__ __forceinline__ void pv256(f32x16* o, int vb0, bf16x8 pa0, bf16x8 pa1, bf16x8 pa2, bf16x8 pa3) {
;     s16x4 xl0, xh0, xl1, xh1, xl2, xh2, xl3, xh3, yl0, yh0, yl1, yh1, yl2, yh2, yl3, yh3;
;     const int va = vb0, vb = vb0 + 16384;
;     asm volatile("s_waitcnt lgkmcnt(0)" ::: "memory");
;     A3_RDK(va, 0, 0); A3_RDK(va, 0, 1); A3_RDK(va, 0, 2); A3_RDK(va, 0, 3);
;     A3_PAIR(o[0], o[1], A3_RDK(va, 2, 0), A3_RDK(va, 2, 1), A3_RDK(va, 2, 2), A3_RDK(va, 2, 3));
;     A3_PAIR(o[2], o[3], A3_RDK(vb, 0, 0), A3_RDK(vb, 0, 1), A3_RDK(vb, 0, 2), A3_RDK(vb, 0, 3));
;     A3_PAIR(o[4], o[5], A3_RDK(vb, 2, 0), A3_RDK(vb, 2, 1), A3_RDK(vb, 2, 2), A3_RDK(vb, 2, 3));
;     A3_PAIR(o[6], o[7], A3_NONE, A3_NONE, A3_NONE, A3_NONE);
; }
.LattB_exit:
	v_add_u32_e32 v147, s65, v210
	ds_read_b64_tr_b16 v[148:149], v147 offset:0
	ds_read_b64_tr_b16 v[150:151], v147 offset:0x800
	ds_read_b64_tr_b16 v[152:153], v147 offset:0x200
	ds_read_b64_tr_b16 v[154:155], v147 offset:0xa00
	ds_read_b64_tr_b16 v[156:157], v147 offset:0x1000
	ds_read_b64_tr_b16 v[158:159], v147 offset:0x1800
	ds_read_b64_tr_b16 v[212:213], v147 offset:0x1200
	ds_read_b64_tr_b16 v[214:215], v147 offset:0x1a00
	ds_read_b64_tr_b16 v[216:217], v147 offset:0x2000
	ds_read_b64_tr_b16 v[218:219], v147 offset:0x2800
	ds_read_b64_tr_b16 v[220:221], v147 offset:0x2200
	ds_read_b64_tr_b16 v[222:223], v147 offset:0x2a00
	ds_read_b64_tr_b16 v[224:225], v147 offset:0x3000
	ds_read_b64_tr_b16 v[226:227], v147 offset:0x3800
	ds_read_b64_tr_b16 v[228:229], v147 offset:0x3200
	ds_read_b64_tr_b16 v[230:231], v147 offset:0x3a00
	s_waitcnt lgkmcnt(12)
	v_add_u32_e32 v160, 0x4000, v147
	v_mfma_f32_32x32x16_bf16 v[114:129], v[142:145], v[148:151], v[114:129]
	v_mfma_f32_32x32x16_bf16 v[98:113], v[142:145], v[152:155], v[98:113]
	ds_read_b64_tr_b16 v[148:149], v147 offset:0x400
	ds_read_b64_tr_b16 v[150:151], v147 offset:0xc00
	ds_read_b64_tr_b16 v[152:153], v147 offset:0x600
	ds_read_b64_tr_b16 v[154:155], v147 offset:0xe00
	s_waitcnt lgkmcnt(12)
	v_mfma_f32_32x32x16_bf16 v[114:129], v[138:141], v[156:159], v[114:129]
	v_mfma_f32_32x32x16_bf16 v[98:113], v[138:141], v[212:215], v[98:113]
	ds_read_b64_tr_b16 v[156:157], v147 offset:0x1400
	ds_read_b64_tr_b16 v[158:159], v147 offset:0x1c00
	ds_read_b64_tr_b16 v[212:213], v147 offset:0x1600
	ds_read_b64_tr_b16 v[214:215], v147 offset:0x1e00
	s_waitcnt lgkmcnt(12)
	v_mfma_f32_32x32x16_bf16 v[114:129], v[134:137], v[216:219], v[114:129]
	v_mfma_f32_32x32x16_bf16 v[98:113], v[134:137], v[220:223], v[98:113]
	ds_read_b64_tr_b16 v[216:217], v147 offset:0x2400
	ds_read_b64_tr_b16 v[218:219], v147 offset:0x2c00
	ds_read_b64_tr_b16 v[220:221], v147 offset:0x2600
	ds_read_b64_tr_b16 v[222:223], v147 offset:0x2e00
	s_waitcnt lgkmcnt(12)
	v_mfma_f32_32x32x16_bf16 v[114:129], v[130:133], v[224:227], v[114:129]
	v_mfma_f32_32x32x16_bf16 v[98:113], v[130:133], v[228:231], v[98:113]
	ds_read_b64_tr_b16 v[224:225], v147 offset:0x3400
	ds_read_b64_tr_b16 v[226:227], v147 offset:0x3c00
	ds_read_b64_tr_b16 v[228:229], v147 offset:0x3600
	ds_read_b64_tr_b16 v[230:231], v147 offset:0x3e00
	s_waitcnt lgkmcnt(12)
	v_mfma_f32_32x32x16_bf16 v[82:97], v[142:145], v[148:151], v[82:97]
	v_mfma_f32_32x32x16_bf16 v[66:81], v[142:145], v[152:155], v[66:81]
	ds_read_b64_tr_b16 v[148:149], v160 offset:0
	ds_read_b64_tr_b16 v[150:151], v160 offset:0x800
	ds_read_b64_tr_b16 v[152:153], v160 offset:0x200
	ds_read_b64_tr_b16 v[154:155], v160 offset:0xa00
	s_waitcnt lgkmcnt(12)
	v_mfma_f32_32x32x16_bf16 v[82:97], v[138:141], v[156:159], v[82:97]
	v_mfma_f32_32x32x16_bf16 v[66:81], v[138:141], v[212:215], v[66:81]
	ds_read_b64_tr_b16 v[156:157], v160 offset:0x1000
	ds_read_b64_tr_b16 v[158:159], v160 offset:0x1800
	ds_read_b64_tr_b16 v[212:213], v160 offset:0x1200
	ds_read_b64_tr_b16 v[214:215], v160 offset:0x1a00
	s_waitcnt lgkmcnt(12)
	v_mfma_f32_32x32x16_bf16 v[82:97], v[134:137], v[216:219], v[82:97]
	v_mfma_f32_32x32x16_bf16 v[66:81], v[134:137], v[220:223], v[66:81]
	ds_read_b64_tr_b16 v[216:217], v160 offset:0x2000
	ds_read_b64_tr_b16 v[218:219], v160 offset:0x2800
	ds_read_b64_tr_b16 v[220:221], v160 offset:0x2200
	ds_read_b64_tr_b16 v[222:223], v160 offset:0x2a00
	s_waitcnt lgkmcnt(12)
	v_mfma_f32_32x32x16_bf16 v[82:97], v[130:133], v[224:227], v[82:97]
	v_mfma_f32_32x32x16_bf16 v[66:81], v[130:133], v[228:231], v[66:81]
	ds_read_b64_tr_b16 v[224:225], v160 offset:0x3000
	ds_read_b64_tr_b16 v[226:227], v160 offset:0x3800
	ds_read_b64_tr_b16 v[228:229], v160 offset:0x3200
	ds_read_b64_tr_b16 v[230:231], v160 offset:0x3a00
	s_waitcnt lgkmcnt(12)
	v_mfma_f32_32x32x16_bf16 v[50:65], v[142:145], v[148:151], v[50:65]
	v_mfma_f32_32x32x16_bf16 v[34:49], v[142:145], v[152:155], v[34:49]
	ds_read_b64_tr_b16 v[148:149], v160 offset:0x400
	ds_read_b64_tr_b16 v[150:151], v160 offset:0xc00
	ds_read_b64_tr_b16 v[152:153], v160 offset:0x600
	ds_read_b64_tr_b16 v[154:155], v160 offset:0xe00
	s_waitcnt lgkmcnt(12)
	v_mfma_f32_32x32x16_bf16 v[50:65], v[138:141], v[156:159], v[50:65]
	v_mfma_f32_32x32x16_bf16 v[34:49], v[138:141], v[212:215], v[34:49]
	ds_read_b64_tr_b16 v[156:157], v160 offset:0x1400
	ds_read_b64_tr_b16 v[158:159], v160 offset:0x1c00
	ds_read_b64_tr_b16 v[212:213], v160 offset:0x1600
	ds_read_b64_tr_b16 v[214:215], v160 offset:0x1e00
	s_waitcnt lgkmcnt(12)
	v_mfma_f32_32x32x16_bf16 v[50:65], v[134:137], v[216:219], v[50:65]
	v_mfma_f32_32x32x16_bf16 v[34:49], v[134:137], v[220:223], v[34:49]
	ds_read_b64_tr_b16 v[216:217], v160 offset:0x2400
	ds_read_b64_tr_b16 v[218:219], v160 offset:0x2c00
	ds_read_b64_tr_b16 v[220:221], v160 offset:0x2600
	ds_read_b64_tr_b16 v[222:223], v160 offset:0x2e00
	s_waitcnt lgkmcnt(12)
	v_mfma_f32_32x32x16_bf16 v[50:65], v[130:133], v[224:227], v[50:65]
	v_mfma_f32_32x32x16_bf16 v[34:49], v[130:133], v[228:231], v[34:49]
	ds_read_b64_tr_b16 v[224:225], v160 offset:0x3400
	ds_read_b64_tr_b16 v[226:227], v160 offset:0x3c00
	ds_read_b64_tr_b16 v[228:229], v160 offset:0x3600
	ds_read_b64_tr_b16 v[230:231], v160 offset:0x3e00
	s_waitcnt lgkmcnt(12)
	v_mfma_f32_32x32x16_bf16 v[18:33], v[142:145], v[148:151], v[18:33]
	v_mfma_f32_32x32x16_bf16 v[2:17], v[142:145], v[152:155], v[2:17]
	s_waitcnt lgkmcnt(0)
	s_waitcnt lgkmcnt(12)
	v_mfma_f32_32x32x16_bf16 v[18:33], v[138:141], v[156:159], v[18:33]
	v_mfma_f32_32x32x16_bf16 v[2:17], v[138:141], v[212:215], v[2:17]
	s_waitcnt lgkmcnt(0)
	s_waitcnt lgkmcnt(12)
	v_mfma_f32_32x32x16_bf16 v[18:33], v[134:137], v[216:219], v[18:33]
	v_mfma_f32_32x32x16_bf16 v[2:17], v[134:137], v[220:223], v[2:17]
	s_waitcnt lgkmcnt(0)
	s_waitcnt lgkmcnt(12)
	v_mfma_f32_32x32x16_bf16 v[18:33], v[130:133], v[224:227], v[18:33]
	v_mfma_f32_32x32x16_bf16 v[2:17], v[130:133], v[228:231], v[2:17]
	s_waitcnt lgkmcnt(0)
	s_branch .LBB0_338
